# baseline (speedup 1.0000x reference)
.LBB4_16:
	s_waitcnt lgkmcnt(8)
	s_barrier
	s_waitcnt lgkmcnt(0)
	s_setprio 1
	s_waitcnt lgkmcnt(0)
	v_mfma_f32_16x16x32_f16 v[74:77], v[14:17], v[30:33], 0
	v_mfma_f32_16x16x32_f16 v[78:81], v[18:21], v[34:37], v[74:77]
	v_mfma_f32_16x16x32_f16 v[74:77], v[6:9], v[22:25], 0
	v_mfma_f32_16x16x32_f16 v[54:57], v[6:9], v[46:49], 0
	v_mfma_f32_16x16x32_f16 v[58:61], v[14:17], v[46:49], 0
	v_mfma_f32_16x16x32_f16 v[62:65], v[6:9], v[38:41], 0
	v_mfma_f32_16x16x32_f16 v[66:69], v[14:17], v[38:41], 0
	v_mfma_f32_16x16x32_f16 v[70:73], v[6:9], v[30:33], 0
	v_mfma_f32_16x16x32_f16 v[82:85], v[10:13], v[26:29], v[74:77]
	v_mfma_f32_16x16x32_f16 v[74:77], v[14:17], v[22:25], 0
	v_mfma_f32_16x16x32_f16 v[54:57], v[10:13], v[50:53], v[54:57]
	v_mfma_f32_16x16x32_f16 v[58:61], v[18:21], v[50:53], v[58:61]
	v_mfma_f32_16x16x32_f16 v[62:65], v[10:13], v[42:45], v[62:65]
	v_mfma_f32_16x16x32_f16 v[66:69], v[18:21], v[42:45], v[66:69]
	v_mfma_f32_16x16x32_f16 v[70:73], v[10:13], v[34:37], v[70:73]
	v_mfma_f32_16x16x32_f16 v[90:93], v[18:21], v[26:29], v[74:77]
	s_setprio 0
	s_barrier
	s_andn2_b64 vcc, exec, s[42:43]
	s_cbranch_vccnz .LBB4_18
	v_mov_b32_e32 v74, v0
	s_lshl_b32 s50, s79, 8
	v_ashrrev_i32_e32 v76, 31, v74
	v_lshrrev_b32_e32 v76, 26, v76
	v_lshlrev_b32_e32 v75, 4, v74
	v_add_u32_e32 v76, v74, v76
	v_bfe_i32 v74, v74, 27, 1
	v_lshrrev_b32_e32 v74, 22, v74
	v_add_u32_e32 v74, v75, v74
	v_and_b32_e32 v74, 0xfffffc00, v74
	v_sub_u32_e32 v74, v75, v74
	v_lshrrev_b32_e32 v75, 4, v74
	v_ashrrev_i32_e32 v77, 31, v74
	v_ashrrev_i32_e32 v76, 6, v76
	v_and_b32_e32 v75, 32, v75
	v_lshrrev_b32_e32 v77, 26, v77
	s_ashr_i32 s51, s50, 31
	v_lshlrev_b32_e32 v76, 3, v76
	v_xad_u32 v74, v75, v74, v77
	v_and_b32_e32 v76, 0x3ffffff0, v76
	v_ashrrev_i32_e32 v74, 6, v74
	s_lshl_b64 s[50:51], s[50:51], 1
	s_add_u32 s50, s26, s50
	v_add_lshl_u32 v74, v74, v76, 2
	s_addc_u32 s51, s27, s51
	v_ashrrev_i32_e32 v75, 31, v74
	v_lshl_add_u64 v[222:223], v[74:75], 1, s[50:51]

.Lhka_done_a0:
	s_andn2_b64 vcc, exec, s[42:43]
	s_cbranch_vccnz .Ltoka_skip
	global_load_dwordx2 v[222:223], v[222:223], off

.LBB5_16:
	s_waitcnt lgkmcnt(8)
	s_barrier
	s_waitcnt lgkmcnt(0)
	s_setprio 1
	s_waitcnt lgkmcnt(0)
	v_mfma_f32_16x16x32_f16 v[54:57], v[6:9], v[46:49], 0
	v_mfma_f32_16x16x32_f16 v[58:61], v[14:17], v[46:49], 0
	v_mfma_f32_16x16x32_f16 v[62:65], v[6:9], v[38:41], 0
	v_mfma_f32_16x16x32_f16 v[66:69], v[14:17], v[38:41], 0
	v_mfma_f32_16x16x32_f16 v[70:73], v[6:9], v[30:33], 0
	v_mfma_f32_16x16x32_f16 v[74:77], v[14:17], v[30:33], 0
	v_mfma_f32_16x16x32_f16 v[78:81], v[6:9], v[22:25], 0
	v_mfma_f32_16x16x32_f16 v[82:85], v[14:17], v[22:25], 0
	v_mfma_f32_16x16x32_f16 v[54:57], v[10:13], v[50:53], v[54:57]
	v_mfma_f32_16x16x32_f16 v[58:61], v[18:21], v[50:53], v[58:61]
	v_mfma_f32_16x16x32_f16 v[62:65], v[10:13], v[42:45], v[62:65]
	v_mfma_f32_16x16x32_f16 v[66:69], v[18:21], v[42:45], v[66:69]
	v_mfma_f32_16x16x32_f16 v[70:73], v[10:13], v[34:37], v[70:73]
	v_mfma_f32_16x16x32_f16 v[74:77], v[18:21], v[34:37], v[74:77]
	v_mfma_f32_16x16x32_f16 v[78:81], v[10:13], v[26:29], v[78:81]
	v_mfma_f32_16x16x32_f16 v[86:89], v[18:21], v[26:29], v[82:85]
	s_setprio 0
	s_barrier
	s_andn2_b64 vcc, exec, s[38:39]
	s_cbranch_vccnz .LBB5_18
	v_mov_b32_e32 v82, v0
	s_lshl_b32 s46, s75, 8
	v_ashrrev_i32_e32 v84, 31, v82
	v_lshrrev_b32_e32 v84, 26, v84
	v_lshlrev_b32_e32 v83, 4, v82
	v_add_u32_e32 v84, v82, v84
	v_bfe_i32 v82, v82, 27, 1
	v_lshrrev_b32_e32 v82, 22, v82
	v_add_u32_e32 v82, v83, v82
	v_and_b32_e32 v82, 0xfffffc00, v82
	v_sub_u32_e32 v82, v83, v82
	v_lshrrev_b32_e32 v83, 4, v82
	v_ashrrev_i32_e32 v85, 31, v82
	v_ashrrev_i32_e32 v84, 6, v84
	v_and_b32_e32 v83, 32, v83
	v_lshrrev_b32_e32 v85, 26, v85
	s_ashr_i32 s47, s46, 31
	v_lshlrev_b32_e32 v84, 3, v84
	v_xad_u32 v82, v83, v82, v85
	v_and_b32_e32 v84, 0x3ffffff0, v84
	v_ashrrev_i32_e32 v82, 6, v82
	s_lshl_b64 s[46:47], s[46:47], 1
	s_add_u32 s46, s22, s46
	v_add_lshl_u32 v82, v82, v84, 2
	s_addc_u32 s47, s23, s47
	v_ashrrev_i32_e32 v83, 31, v82
	v_lshl_add_u64 v[218:219], v[82:83], 1, s[46:47]

.Lhkb_done_b0:
	s_andn2_b64 vcc, exec, s[38:39]
	s_cbranch_vccnz .Ltokb_skip
	global_load_dwordx2 v[218:219], v[218:219], off
